# EpiDown: column scale and bias vectors read from the LDS parameter block once per unit instead of every row step
# speedup vs baseline: 1.0018x; 1.0018x over previous
; #define GAS __attribute__((address_space(1)))
; #define LAS __attribute__((address_space(3)))
; #define EPI_LOOP_AM for (int ai = 0; ai < 2; ++ai) _Pragma("unroll") for (int m = 0; m < 4; ++m)
; #define EPI_FENCE __builtin_amdgcn_sched_barrier(0)
;     __device__ __forceinline__ void operator()(Acc& acc, const Unit& u, LAS unsigned char* lds, int wr, int wc, int fr, int fq) const {
;         const int rt = u.p0, pn = u.p1, c0 = pn * 256 + wc * 32 + 8 * fq;
;         const LAS float* blk = (const LAS float*)(lds + LDS_STAGE + u.q * 4096);
; #pragma unroll
;         for (int bj = 0; bj < 2; ++bj) { const int cc = 128 * bj + wc * 32 + 8 * fq;
; #pragma unroll
;             EPI_LOOP_AM { const int r = 128 * ai + 64 * wr + 16 * m + fr;
;                 const f32x4 w0 = *(const LAS f32x4*)(blk + 256 + cc) * 0.25f, w1 = *(const LAS f32x4*)(blk + 256 + cc + 4) * 0.25f, b0 = *(const LAS f32x4*)(blk + 512 + cc), b1 = *(const LAS f32x4*)(blk + 512 + cc + 4);
;                 f32x4 y0 = (acc[ai][bj][m][0] * w0 + b0) * 32.f, y1 = (acc[ai][bj][m][1] * w1 + b1) * 32.f;
; #pragma unroll
;                 for (int j = 0; j < 4; ++j) { y0[j] = fminf(fmaxf(y0[j], -440.f), 440.f); y1[j] = fminf(fmaxf(y1[j], -440.f), 440.f); }
;                 int p0 = __builtin_amdgcn_cvt_pk_fp8_f32(y0[0], y0[1], 0, false); p0 = __builtin_amdgcn_cvt_pk_fp8_f32(y0[2], y0[3], p0, true);
;                 int p1 = __builtin_amdgcn_cvt_pk_fp8_f32(y1[0], y1[1], 0, false); p1 = __builtin_amdgcn_cvt_pk_fp8_f32(y1[2], y1[3], p1, true);
;                 *(GAS v2u*)(yr8 + ((size_t)rt * 256 + r) * D + c0 + 128 * bj) = (v2u){(unsigned)p0, (unsigned)p1}; EPI_FENCE; } }
;     }
.LBB0_1737:
	s_lshl_b32 s29, s73, 12
	v_mov_b32_e32 v128, v254
	v_mov_b32_e32 v130, v136
	s_add_i32 s29, s29, 0
	s_add_i32 s29, s29, 0x20000
	v_lshl_add_u32 v131, v130, 3, s61
	v_add_u32_e32 v132, s60, v128
	v_lshl_add_u32 v128, v131, 2, s29
	ds_read_b128 v[160:163], v128 offset:1024
	ds_read_b128 v[164:167], v128 offset:1040
	ds_read_b128 v[168:171], v128 offset:2048
	ds_read_b128 v[172:175], v128 offset:2064
	ds_read_b128 v[176:179], v128 offset:1536
	ds_read_b128 v[180:183], v128 offset:1552
	ds_read_b128 v[184:187], v128 offset:2560
	ds_read_b128 v[188:191], v128 offset:2576
	v_lshl_add_u32 v130, s43, 8, v131
	s_ashr_i32 s43, s42, 31
	s_waitcnt lgkmcnt(0)
	v_pk_mul_f32 v[134:135], v[162:163], s[16:17] op_sel_hi:[1,0]
	v_pk_mul_f32 v[154:155], v[160:161], s[16:17] op_sel_hi:[1,0]
	v_pk_mul_f32 v[146:147], v[164:165], s[16:17] op_sel_hi:[1,0]
	v_pk_fma_f32 v[124:125], v[124:125], v[154:155], v[168:169]
	v_pk_mul_f32 v[148:149], v[166:167], s[16:17] op_sel_hi:[1,0]
	v_pk_mul_f32 v[124:125], v[124:125], s[18:19] op_sel_hi:[1,0]
	s_waitcnt lgkmcnt(0)
	v_pk_fma_f32 v[120:121], v[120:121], v[146:147], v[172:173]
	v_med3_f32 v133, v124, s68, v140
	v_pk_mul_f32 v[120:121], v[120:121], s[18:19] op_sel_hi:[1,0]
	v_med3_f32 v125, v125, s68, v140
	v_mov_b32_e32 v124, v129
	v_med3_f32 v120, v120, s68, v140
	v_med3_f32 v121, v121, s68, v140
	v_cvt_pk_fp8_f32 v124, v133, v125
	v_mov_b32_e32 v125, v129
	v_cvt_pk_fp8_f32 v125, v120, v121
	v_pk_fma_f32 v[126:127], v[126:127], v[134:135], v[170:171]
	v_pk_fma_f32 v[122:123], v[122:123], v[148:149], v[174:175]
	v_pk_mul_f32 v[126:127], v[126:127], s[18:19] op_sel_hi:[1,0]
	v_pk_mul_f32 v[122:123], v[122:123], s[18:19] op_sel_hi:[1,0]
	s_lshl_b64 s[42:43], s[42:43], 19
	v_med3_f32 v126, v126, s68, v140
	v_med3_f32 v122, v122, s68, v140
	v_med3_f32 v120, v127, s68, v140
	v_med3_f32 v121, v123, s68, v140
	v_cvt_pk_fp8_f32 v124, v126, v120 op_sel:[0,0,1]
	v_cvt_pk_fp8_f32 v125, v122, v121 op_sel:[0,0,1]
	v_ashrrev_i32_e32 v133, 31, v132
	s_add_u32 s42, s27, s42
	v_lshlrev_b64 v[120:121], 11, v[132:133]
	s_addc_u32 s43, s33, s43
	v_ashrrev_i32_e32 v131, 31, v130
	v_lshl_add_u64 v[120:121], s[42:43], 0, v[120:121]
	v_lshl_add_u64 v[120:121], v[120:121], 0, v[130:131]
	global_store_dwordx2 v[120:121], v[124:125], off
	s_waitcnt lgkmcnt(0)
	v_pk_mul_f32 v[126:127], v[162:163], s[16:17] op_sel_hi:[1,0]
	v_pk_mul_f32 v[134:135], v[160:161], s[16:17] op_sel_hi:[1,0]
	v_pk_mul_f32 v[142:143], v[164:165], s[16:17] op_sel_hi:[1,0]
	v_pk_fma_f32 v[116:117], v[116:117], v[134:135], v[168:169]
	v_pk_mul_f32 v[144:145], v[166:167], s[16:17] op_sel_hi:[1,0]
	v_pk_mul_f32 v[116:117], v[116:117], s[18:19] op_sel_hi:[1,0]
	s_waitcnt lgkmcnt(0)
	v_pk_fma_f32 v[112:113], v[112:113], v[142:143], v[172:173]
	v_med3_f32 v122, v116, s68, v140
	v_pk_mul_f32 v[112:113], v[112:113], s[18:19] op_sel_hi:[1,0]
	v_med3_f32 v117, v117, s68, v140
	v_mov_b32_e32 v116, v129
	v_med3_f32 v112, v112, s68, v140
	v_med3_f32 v113, v113, s68, v140
	v_cvt_pk_fp8_f32 v116, v122, v117
	v_mov_b32_e32 v117, v129
	v_cvt_pk_fp8_f32 v117, v112, v113
	v_pk_fma_f32 v[118:119], v[118:119], v[126:127], v[170:171]
	v_pk_fma_f32 v[114:115], v[114:115], v[144:145], v[174:175]
	v_pk_mul_f32 v[118:119], v[118:119], s[18:19] op_sel_hi:[1,0]
	v_pk_mul_f32 v[114:115], v[114:115], s[18:19] op_sel_hi:[1,0]
	v_med3_f32 v118, v118, s68, v140
	v_med3_f32 v114, v114, s68, v140
	v_med3_f32 v119, v119, s68, v140
	v_med3_f32 v113, v115, s68, v140
	v_add_u32_e32 v112, 16, v132
	v_cvt_pk_fp8_f32 v116, v118, v119 op_sel:[0,0,1]
	v_cvt_pk_fp8_f32 v117, v114, v113 op_sel:[0,0,1]
	v_ashrrev_i32_e32 v113, 31, v112
	v_lshlrev_b64 v[112:113], 11, v[112:113]
	v_lshl_add_u64 v[112:113], s[42:43], 0, v[112:113]
	v_lshl_add_u64 v[112:113], v[112:113], 0, v[130:131]
	global_store_dwordx2 v[112:113], v[116:117], off
	s_waitcnt lgkmcnt(0)
	v_pk_mul_f32 v[118:119], v[162:163], s[16:17] op_sel_hi:[1,0]
	v_pk_mul_f32 v[126:127], v[160:161], s[16:17] op_sel_hi:[1,0]
	v_pk_mul_f32 v[122:123], v[164:165], s[16:17] op_sel_hi:[1,0]
	v_pk_fma_f32 v[108:109], v[108:109], v[126:127], v[168:169]
	v_pk_mul_f32 v[124:125], v[166:167], s[16:17] op_sel_hi:[1,0]
	v_pk_mul_f32 v[108:109], v[108:109], s[18:19] op_sel_hi:[1,0]
	s_waitcnt lgkmcnt(0)
	v_pk_fma_f32 v[104:105], v[104:105], v[122:123], v[172:173]
	v_med3_f32 v114, v108, s68, v140
	v_pk_mul_f32 v[104:105], v[104:105], s[18:19] op_sel_hi:[1,0]
	v_med3_f32 v109, v109, s68, v140
	v_mov_b32_e32 v108, v129
	v_med3_f32 v104, v104, s68, v140
	v_med3_f32 v105, v105, s68, v140
	v_cvt_pk_fp8_f32 v108, v114, v109
	v_mov_b32_e32 v109, v129
	v_cvt_pk_fp8_f32 v109, v104, v105
	v_pk_fma_f32 v[110:111], v[110:111], v[118:119], v[170:171]
	v_pk_fma_f32 v[106:107], v[106:107], v[124:125], v[174:175]
	v_pk_mul_f32 v[110:111], v[110:111], s[18:19] op_sel_hi:[1,0]
	v_pk_mul_f32 v[106:107], v[106:107], s[18:19] op_sel_hi:[1,0]
	v_med3_f32 v110, v110, s68, v140
	v_med3_f32 v106, v106, s68, v140
	v_med3_f32 v111, v111, s68, v140
	v_med3_f32 v105, v107, s68, v140
	v_add_u32_e32 v104, 32, v132
	v_cvt_pk_fp8_f32 v108, v110, v111 op_sel:[0,0,1]
	v_cvt_pk_fp8_f32 v109, v106, v105 op_sel:[0,0,1]
	v_ashrrev_i32_e32 v105, 31, v104
	v_lshlrev_b64 v[104:105], 11, v[104:105]
	v_lshl_add_u64 v[104:105], s[42:43], 0, v[104:105]
	v_lshl_add_u64 v[104:105], v[104:105], 0, v[130:131]
	global_store_dwordx2 v[104:105], v[108:109], off
	s_waitcnt lgkmcnt(0)
	v_pk_mul_f32 v[110:111], v[162:163], s[16:17] op_sel_hi:[1,0]
	v_pk_mul_f32 v[118:119], v[160:161], s[16:17] op_sel_hi:[1,0]
	v_pk_mul_f32 v[114:115], v[164:165], s[16:17] op_sel_hi:[1,0]
	v_pk_fma_f32 v[100:101], v[100:101], v[118:119], v[168:169]
	v_pk_mul_f32 v[116:117], v[166:167], s[16:17] op_sel_hi:[1,0]
	v_pk_mul_f32 v[100:101], v[100:101], s[18:19] op_sel_hi:[1,0]
	s_waitcnt lgkmcnt(0)
; #define GAS __attribute__((address_space(1)))
; #define LAS __attribute__((address_space(3)))
; #define EPI_LOOP_AM for (int ai = 0; ai < 2; ++ai) _Pragma("unroll") for (int m = 0; m < 4; ++m)
; #define EPI_FENCE __builtin_amdgcn_sched_barrier(0)
;     __device__ __forceinline__ void operator()(Acc& acc, const Unit& u, LAS unsigned char* lds, int wr, int wc, int fr, int fq) const {
;         const int rt = u.p0, pn = u.p1, c0 = pn * 256 + wc * 32 + 8 * fq;
;         const LAS float* blk = (const LAS float*)(lds + LDS_STAGE + u.q * 4096);
; #pragma unroll
;         for (int bj = 0; bj < 2; ++bj) { const int cc = 128 * bj + wc * 32 + 8 * fq;
; #pragma unroll
;             EPI_LOOP_AM { const int r = 128 * ai + 64 * wr + 16 * m + fr;
;                 const f32x4 w0 = *(const LAS f32x4*)(blk + 256 + cc) * 0.25f, w1 = *(const LAS f32x4*)(blk + 256 + cc + 4) * 0.25f, b0 = *(const LAS f32x4*)(blk + 512 + cc), b1 = *(const LAS f32x4*)(blk + 512 + cc + 4);
;                 f32x4 y0 = (acc[ai][bj][m][0] * w0 + b0) * 32.f, y1 = (acc[ai][bj][m][1] * w1 + b1) * 32.f;
; #pragma unroll
;                 for (int j = 0; j < 4; ++j) { y0[j] = fminf(fmaxf(y0[j], -440.f), 440.f); y1[j] = fminf(fmaxf(y1[j], -440.f), 440.f); }
;                 int p0 = __builtin_amdgcn_cvt_pk_fp8_f32(y0[0], y0[1], 0, false); p0 = __builtin_amdgcn_cvt_pk_fp8_f32(y0[2], y0[3], p0, true);
;                 int p1 = __builtin_amdgcn_cvt_pk_fp8_f32(y1[0], y1[1], 0, false); p1 = __builtin_amdgcn_cvt_pk_fp8_f32(y1[2], y1[3], p1, true);
;                 *(GAS v2u*)(yr8 + ((size_t)rt * 256 + r) * D + c0 + 128 * bj) = (v2u){(unsigned)p0, (unsigned)p1}; EPI_FENCE; } }
;     }
	v_pk_fma_f32 v[96:97], v[96:97], v[114:115], v[172:173]
	v_med3_f32 v106, v100, s68, v140
	v_pk_mul_f32 v[96:97], v[96:97], s[18:19] op_sel_hi:[1,0]
	v_med3_f32 v101, v101, s68, v140
	v_mov_b32_e32 v100, v129
	v_med3_f32 v96, v96, s68, v140
	v_med3_f32 v97, v97, s68, v140
	v_cvt_pk_fp8_f32 v100, v106, v101
	v_mov_b32_e32 v101, v129
	v_cvt_pk_fp8_f32 v101, v96, v97
	v_pk_fma_f32 v[102:103], v[102:103], v[110:111], v[170:171]
	v_pk_fma_f32 v[98:99], v[98:99], v[116:117], v[174:175]
	v_pk_mul_f32 v[102:103], v[102:103], s[18:19] op_sel_hi:[1,0]
	v_pk_mul_f32 v[98:99], v[98:99], s[18:19] op_sel_hi:[1,0]
	v_med3_f32 v102, v102, s68, v140
	v_med3_f32 v98, v98, s68, v140
	v_med3_f32 v103, v103, s68, v140
	v_med3_f32 v97, v99, s68, v140
	v_add_u32_e32 v96, 48, v132
	v_cvt_pk_fp8_f32 v100, v102, v103 op_sel:[0,0,1]
	v_cvt_pk_fp8_f32 v101, v98, v97 op_sel:[0,0,1]
	v_ashrrev_i32_e32 v97, 31, v96
	v_lshlrev_b64 v[96:97], 11, v[96:97]
	v_lshl_add_u64 v[96:97], s[42:43], 0, v[96:97]
	v_lshl_add_u64 v[96:97], v[96:97], 0, v[130:131]
	global_store_dwordx2 v[96:97], v[100:101], off
	v_add_u32_e32 v102, 0x80, v132
	v_ashrrev_i32_e32 v103, 31, v102
	s_waitcnt lgkmcnt(0)
	v_pk_mul_f32 v[110:111], v[162:163], s[16:17] op_sel_hi:[1,0]
	v_pk_mul_f32 v[118:119], v[160:161], s[16:17] op_sel_hi:[1,0]
	v_pk_mul_f32 v[106:107], v[164:165], s[16:17] op_sel_hi:[1,0]
	v_pk_fma_f32 v[92:93], v[92:93], v[118:119], v[168:169]
	v_pk_mul_f32 v[108:109], v[166:167], s[16:17] op_sel_hi:[1,0]
	v_pk_mul_f32 v[92:93], v[92:93], s[18:19] op_sel_hi:[1,0]
	s_waitcnt lgkmcnt(0)
	v_pk_fma_f32 v[88:89], v[88:89], v[106:107], v[172:173]
	v_med3_f32 v98, v92, s68, v140
	v_pk_mul_f32 v[88:89], v[88:89], s[18:19] op_sel_hi:[1,0]
	v_med3_f32 v93, v93, s68, v140
	v_mov_b32_e32 v92, v129
	v_med3_f32 v88, v88, s68, v140
	v_med3_f32 v89, v89, s68, v140
	v_cvt_pk_fp8_f32 v92, v98, v93
	v_mov_b32_e32 v93, v129
	v_cvt_pk_fp8_f32 v93, v88, v89
	v_pk_fma_f32 v[94:95], v[94:95], v[110:111], v[170:171]
	v_pk_fma_f32 v[90:91], v[90:91], v[108:109], v[174:175]
	v_pk_mul_f32 v[94:95], v[94:95], s[18:19] op_sel_hi:[1,0]
	v_pk_mul_f32 v[90:91], v[90:91], s[18:19] op_sel_hi:[1,0]
	v_med3_f32 v94, v94, s68, v140
	v_med3_f32 v90, v90, s68, v140
	v_med3_f32 v88, v95, s68, v140
	v_med3_f32 v89, v91, s68, v140
	v_cvt_pk_fp8_f32 v92, v94, v88 op_sel:[0,0,1]
	v_cvt_pk_fp8_f32 v93, v90, v89 op_sel:[0,0,1]
	v_lshlrev_b64 v[88:89], 11, v[102:103]
	v_lshl_add_u64 v[88:89], s[42:43], 0, v[88:89]
	v_lshl_add_u64 v[88:89], v[88:89], 0, v[130:131]
	global_store_dwordx2 v[88:89], v[92:93], off
	s_waitcnt lgkmcnt(0)
	v_pk_mul_f32 v[94:95], v[162:163], s[16:17] op_sel_hi:[1,0]
	v_pk_mul_f32 v[102:103], v[160:161], s[16:17] op_sel_hi:[1,0]
	v_pk_mul_f32 v[98:99], v[164:165], s[16:17] op_sel_hi:[1,0]
	v_pk_fma_f32 v[84:85], v[84:85], v[102:103], v[168:169]
	v_pk_mul_f32 v[100:101], v[166:167], s[16:17] op_sel_hi:[1,0]
	v_pk_mul_f32 v[84:85], v[84:85], s[18:19] op_sel_hi:[1,0]
	s_waitcnt lgkmcnt(0)
	v_pk_fma_f32 v[80:81], v[80:81], v[98:99], v[172:173]
	v_med3_f32 v90, v84, s68, v140
	v_pk_mul_f32 v[80:81], v[80:81], s[18:19] op_sel_hi:[1,0]
	v_med3_f32 v85, v85, s68, v140
	v_mov_b32_e32 v84, v129
	v_med3_f32 v80, v80, s68, v140
	v_med3_f32 v81, v81, s68, v140
	v_cvt_pk_fp8_f32 v84, v90, v85
	v_mov_b32_e32 v85, v129
	v_cvt_pk_fp8_f32 v85, v80, v81
	v_pk_fma_f32 v[86:87], v[86:87], v[94:95], v[170:171]
	v_pk_fma_f32 v[82:83], v[82:83], v[100:101], v[174:175]
	v_pk_mul_f32 v[86:87], v[86:87], s[18:19] op_sel_hi:[1,0]
	v_pk_mul_f32 v[82:83], v[82:83], s[18:19] op_sel_hi:[1,0]
	v_med3_f32 v86, v86, s68, v140
	v_med3_f32 v82, v82, s68, v140
	v_med3_f32 v87, v87, s68, v140
	v_med3_f32 v81, v83, s68, v140
	v_add_u32_e32 v80, 0x90, v132
	v_cvt_pk_fp8_f32 v84, v86, v87 op_sel:[0,0,1]
	v_cvt_pk_fp8_f32 v85, v82, v81 op_sel:[0,0,1]
	v_ashrrev_i32_e32 v81, 31, v80
	v_lshlrev_b64 v[80:81], 11, v[80:81]
	v_lshl_add_u64 v[80:81], s[42:43], 0, v[80:81]
	v_lshl_add_u64 v[80:81], v[80:81], 0, v[130:131]
	global_store_dwordx2 v[80:81], v[84:85], off
	s_waitcnt lgkmcnt(0)
	v_pk_mul_f32 v[86:87], v[162:163], s[16:17] op_sel_hi:[1,0]
	v_pk_mul_f32 v[94:95], v[160:161], s[16:17] op_sel_hi:[1,0]
	v_pk_mul_f32 v[90:91], v[164:165], s[16:17] op_sel_hi:[1,0]
	v_pk_fma_f32 v[76:77], v[76:77], v[94:95], v[168:169]
	v_pk_mul_f32 v[92:93], v[166:167], s[16:17] op_sel_hi:[1,0]
	v_pk_mul_f32 v[76:77], v[76:77], s[18:19] op_sel_hi:[1,0]
	s_waitcnt lgkmcnt(0)
	v_pk_fma_f32 v[72:73], v[72:73], v[90:91], v[172:173]
	v_med3_f32 v82, v76, s68, v140
	v_pk_mul_f32 v[72:73], v[72:73], s[18:19] op_sel_hi:[1,0]
	v_med3_f32 v77, v77, s68, v140
	v_mov_b32_e32 v76, v129
	v_med3_f32 v72, v72, s68, v140
	v_med3_f32 v73, v73, s68, v140
	v_cvt_pk_fp8_f32 v76, v82, v77
	v_mov_b32_e32 v77, v129
	v_cvt_pk_fp8_f32 v77, v72, v73
	v_pk_fma_f32 v[78:79], v[78:79], v[86:87], v[170:171]
	v_pk_fma_f32 v[74:75], v[74:75], v[92:93], v[174:175]
	v_pk_mul_f32 v[78:79], v[78:79], s[18:19] op_sel_hi:[1,0]
	v_pk_mul_f32 v[74:75], v[74:75], s[18:19] op_sel_hi:[1,0]
	v_med3_f32 v78, v78, s68, v140
	v_med3_f32 v74, v74, s68, v140
	v_med3_f32 v79, v79, s68, v140
	v_med3_f32 v73, v75, s68, v140
	v_add_u32_e32 v72, 0xa0, v132
	v_cvt_pk_fp8_f32 v76, v78, v79 op_sel:[0,0,1]
	v_cvt_pk_fp8_f32 v77, v74, v73 op_sel:[0,0,1]
	v_ashrrev_i32_e32 v73, 31, v72
	v_lshlrev_b64 v[72:73], 11, v[72:73]
	v_lshl_add_u64 v[72:73], s[42:43], 0, v[72:73]
	v_lshl_add_u64 v[72:73], v[72:73], 0, v[130:131]
	global_store_dwordx2 v[72:73], v[76:77], off
	s_waitcnt lgkmcnt(0)
; #define GAS __attribute__((address_space(1)))
; #define LAS __attribute__((address_space(3)))
; #define EPI_LOOP_AM for (int ai = 0; ai < 2; ++ai) _Pragma("unroll") for (int m = 0; m < 4; ++m)
; #define EPI_FENCE __builtin_amdgcn_sched_barrier(0)
;     __device__ __forceinline__ void operator()(Acc& acc, const Unit& u, LAS unsigned char* lds, int wr, int wc, int fr, int fq) const {
;         const int rt = u.p0, pn = u.p1, c0 = pn * 256 + wc * 32 + 8 * fq;
;         const LAS float* blk = (const LAS float*)(lds + LDS_STAGE + u.q * 4096);
; #pragma unroll
;         for (int bj = 0; bj < 2; ++bj) { const int cc = 128 * bj + wc * 32 + 8 * fq;
; #pragma unroll
;             EPI_LOOP_AM { const int r = 128 * ai + 64 * wr + 16 * m + fr;
;                 const f32x4 w0 = *(const LAS f32x4*)(blk + 256 + cc) * 0.25f, w1 = *(const LAS f32x4*)(blk + 256 + cc + 4) * 0.25f, b0 = *(const LAS f32x4*)(blk + 512 + cc), b1 = *(const LAS f32x4*)(blk + 512 + cc + 4);
;                 f32x4 y0 = (acc[ai][bj][m][0] * w0 + b0) * 32.f, y1 = (acc[ai][bj][m][1] * w1 + b1) * 32.f;
; #pragma unroll
;                 for (int j = 0; j < 4; ++j) { y0[j] = fminf(fmaxf(y0[j], -440.f), 440.f); y1[j] = fminf(fmaxf(y1[j], -440.f), 440.f); }
;                 int p0 = __builtin_amdgcn_cvt_pk_fp8_f32(y0[0], y0[1], 0, false); p0 = __builtin_amdgcn_cvt_pk_fp8_f32(y0[2], y0[3], p0, true);
;                 int p1 = __builtin_amdgcn_cvt_pk_fp8_f32(y1[0], y1[1], 0, false); p1 = __builtin_amdgcn_cvt_pk_fp8_f32(y1[2], y1[3], p1, true);
;                 *(GAS v2u*)(yr8 + ((size_t)rt * 256 + r) * D + c0 + 128 * bj) = (v2u){(unsigned)p0, (unsigned)p1}; EPI_FENCE; } }
;     }
	v_pk_mul_f32 v[78:79], v[162:163], s[16:17] op_sel_hi:[1,0]
	v_pk_mul_f32 v[86:87], v[160:161], s[16:17] op_sel_hi:[1,0]
	v_pk_mul_f32 v[82:83], v[164:165], s[16:17] op_sel_hi:[1,0]
	v_pk_fma_f32 v[68:69], v[68:69], v[86:87], v[168:169]
	v_pk_mul_f32 v[84:85], v[166:167], s[16:17] op_sel_hi:[1,0]
	v_pk_mul_f32 v[68:69], v[68:69], s[18:19] op_sel_hi:[1,0]
	s_waitcnt lgkmcnt(0)
	v_pk_fma_f32 v[64:65], v[64:65], v[82:83], v[172:173]
	v_med3_f32 v74, v68, s68, v140
	v_pk_mul_f32 v[64:65], v[64:65], s[18:19] op_sel_hi:[1,0]
	v_med3_f32 v69, v69, s68, v140
	v_mov_b32_e32 v68, v129
	v_med3_f32 v64, v64, s68, v140
	v_med3_f32 v65, v65, s68, v140
	v_cvt_pk_fp8_f32 v68, v74, v69
	v_mov_b32_e32 v69, v129
	v_cvt_pk_fp8_f32 v69, v64, v65
	v_pk_fma_f32 v[70:71], v[70:71], v[78:79], v[170:171]
	v_pk_fma_f32 v[66:67], v[66:67], v[84:85], v[174:175]
	v_pk_mul_f32 v[70:71], v[70:71], s[18:19] op_sel_hi:[1,0]
	v_pk_mul_f32 v[66:67], v[66:67], s[18:19] op_sel_hi:[1,0]
	v_med3_f32 v70, v70, s68, v140
	v_med3_f32 v66, v66, s68, v140
	v_med3_f32 v71, v71, s68, v140
	v_med3_f32 v65, v67, s68, v140
	v_add_u32_e32 v64, 0xb0, v132
	v_cvt_pk_fp8_f32 v68, v70, v71 op_sel:[0,0,1]
	v_cvt_pk_fp8_f32 v69, v66, v65 op_sel:[0,0,1]
	v_ashrrev_i32_e32 v65, 31, v64
	v_lshlrev_b64 v[64:65], 11, v[64:65]
	v_lshl_add_u64 v[64:65], s[42:43], 0, v[64:65]
	v_lshl_add_u64 v[64:65], v[64:65], 0, v[130:131]
	global_store_dwordx2 v[64:65], v[68:69], off
	s_waitcnt lgkmcnt(0)
	v_pk_mul_f32 v[70:71], v[178:179], s[16:17] op_sel_hi:[1,0]
	v_pk_mul_f32 v[78:79], v[176:177], s[16:17] op_sel_hi:[1,0]
	v_pk_mul_f32 v[74:75], v[180:181], s[16:17] op_sel_hi:[1,0]
	v_pk_fma_f32 v[60:61], v[60:61], v[78:79], v[184:185]
	v_pk_mul_f32 v[76:77], v[182:183], s[16:17] op_sel_hi:[1,0]
	v_pk_mul_f32 v[60:61], v[60:61], s[18:19] op_sel_hi:[1,0]
	s_waitcnt lgkmcnt(0)
	v_pk_fma_f32 v[56:57], v[56:57], v[74:75], v[188:189]
	v_med3_f32 v60, v60, s68, v140
	v_pk_mul_f32 v[56:57], v[56:57], s[18:19] op_sel_hi:[1,0]
	v_med3_f32 v61, v61, s68, v140
	v_med3_f32 v66, v56, s68, v140
	v_med3_f32 v67, v57, s68, v140
	v_mov_b32_e32 v56, v129
	v_mov_b32_e32 v57, v129
	v_cvt_pk_fp8_f32 v56, v60, v61
	v_cvt_pk_fp8_f32 v57, v66, v67
	v_pk_fma_f32 v[62:63], v[62:63], v[70:71], v[186:187]
	v_pk_fma_f32 v[58:59], v[58:59], v[76:77], v[190:191]
	v_pk_mul_f32 v[62:63], v[62:63], s[18:19] op_sel_hi:[1,0]
	v_pk_mul_f32 v[58:59], v[58:59], s[18:19] op_sel_hi:[1,0]
	v_med3_f32 v62, v62, s68, v140
	v_med3_f32 v58, v58, s68, v140
	v_med3_f32 v60, v63, s68, v140
	v_med3_f32 v59, v59, s68, v140
	v_cvt_pk_fp8_f32 v56, v62, v60 op_sel:[0,0,1]
	v_cvt_pk_fp8_f32 v57, v58, v59 op_sel:[0,0,1]
	global_store_dwordx2 v[120:121], v[56:57], off offset:128
	s_waitcnt lgkmcnt(0)
	v_pk_mul_f32 v[70:71], v[178:179], s[16:17] op_sel_hi:[1,0]
	v_pk_mul_f32 v[74:75], v[176:177], s[16:17] op_sel_hi:[1,0]
	v_pk_mul_f32 v[60:61], v[180:181], s[16:17] op_sel_hi:[1,0]
	v_pk_fma_f32 v[52:53], v[52:53], v[74:75], v[184:185]
	v_pk_mul_f32 v[62:63], v[182:183], s[16:17] op_sel_hi:[1,0]
	v_pk_mul_f32 v[52:53], v[52:53], s[18:19] op_sel_hi:[1,0]
	s_waitcnt lgkmcnt(0)
	v_pk_fma_f32 v[48:49], v[48:49], v[60:61], v[188:189]
	v_med3_f32 v52, v52, s68, v140
	v_pk_mul_f32 v[48:49], v[48:49], s[18:19] op_sel_hi:[1,0]
	v_med3_f32 v53, v53, s68, v140
	v_med3_f32 v56, v48, s68, v140
	v_med3_f32 v57, v49, s68, v140
	v_mov_b32_e32 v48, v129
	v_mov_b32_e32 v49, v129
	v_cvt_pk_fp8_f32 v48, v52, v53
	v_cvt_pk_fp8_f32 v49, v56, v57
	v_pk_fma_f32 v[54:55], v[54:55], v[70:71], v[186:187]
	v_pk_fma_f32 v[50:51], v[50:51], v[62:63], v[190:191]
	v_pk_mul_f32 v[54:55], v[54:55], s[18:19] op_sel_hi:[1,0]
	v_pk_mul_f32 v[50:51], v[50:51], s[18:19] op_sel_hi:[1,0]
	v_med3_f32 v54, v54, s68, v140
	v_med3_f32 v50, v50, s68, v140
	v_med3_f32 v52, v55, s68, v140
	v_med3_f32 v51, v51, s68, v140
	v_cvt_pk_fp8_f32 v48, v54, v52 op_sel:[0,0,1]
	v_cvt_pk_fp8_f32 v49, v50, v51 op_sel:[0,0,1]
	global_store_dwordx2 v[112:113], v[48:49], off offset:128
	s_waitcnt lgkmcnt(0)
	v_pk_mul_f32 v[60:61], v[178:179], s[16:17] op_sel_hi:[1,0]
	v_pk_mul_f32 v[62:63], v[176:177], s[16:17] op_sel_hi:[1,0]
	v_pk_mul_f32 v[52:53], v[180:181], s[16:17] op_sel_hi:[1,0]
	v_pk_fma_f32 v[44:45], v[44:45], v[62:63], v[184:185]
	v_pk_mul_f32 v[54:55], v[182:183], s[16:17] op_sel_hi:[1,0]
	v_pk_mul_f32 v[44:45], v[44:45], s[18:19] op_sel_hi:[1,0]
	s_waitcnt lgkmcnt(0)
	v_pk_fma_f32 v[40:41], v[40:41], v[52:53], v[188:189]
	v_med3_f32 v44, v44, s68, v140
	v_pk_mul_f32 v[40:41], v[40:41], s[18:19] op_sel_hi:[1,0]
	v_med3_f32 v45, v45, s68, v140
	v_med3_f32 v48, v40, s68, v140
	v_med3_f32 v49, v41, s68, v140
	v_mov_b32_e32 v40, v129
	v_mov_b32_e32 v41, v129
	v_cvt_pk_fp8_f32 v40, v44, v45
	v_cvt_pk_fp8_f32 v41, v48, v49
	v_pk_fma_f32 v[46:47], v[46:47], v[60:61], v[186:187]
	v_pk_fma_f32 v[42:43], v[42:43], v[54:55], v[190:191]
	v_pk_mul_f32 v[46:47], v[46:47], s[18:19] op_sel_hi:[1,0]
	v_pk_mul_f32 v[42:43], v[42:43], s[18:19] op_sel_hi:[1,0]
	v_med3_f32 v46, v46, s68, v140
	v_med3_f32 v42, v42, s68, v140
	v_med3_f32 v44, v47, s68, v140
	v_med3_f32 v43, v43, s68, v140
	v_cvt_pk_fp8_f32 v40, v46, v44 op_sel:[0,0,1]
	v_cvt_pk_fp8_f32 v41, v42, v43 op_sel:[0,0,1]
	global_store_dwordx2 v[104:105], v[40:41], off offset:128
	s_waitcnt lgkmcnt(0)
	v_pk_mul_f32 v[52:53], v[178:179], s[16:17] op_sel_hi:[1,0]
	v_pk_mul_f32 v[54:55], v[176:177], s[16:17] op_sel_hi:[1,0]
	v_pk_mul_f32 v[44:45], v[180:181], s[16:17] op_sel_hi:[1,0]
	v_pk_fma_f32 v[36:37], v[36:37], v[54:55], v[184:185]
	v_pk_mul_f32 v[46:47], v[182:183], s[16:17] op_sel_hi:[1,0]
	v_pk_mul_f32 v[36:37], v[36:37], s[18:19] op_sel_hi:[1,0]
	s_waitcnt lgkmcnt(0)
; #define GAS __attribute__((address_space(1)))
; #define LAS __attribute__((address_space(3)))
; #define EPI_LOOP_AM for (int ai = 0; ai < 2; ++ai) _Pragma("unroll") for (int m = 0; m < 4; ++m)
; #define EPI_FENCE __builtin_amdgcn_sched_barrier(0)
;     __device__ __forceinline__ void operator()(Acc& acc, const Unit& u, LAS unsigned char* lds, int wr, int wc, int fr, int fq) const {
;         const int rt = u.p0, pn = u.p1, c0 = pn * 256 + wc * 32 + 8 * fq;
;         const LAS float* blk = (const LAS float*)(lds + LDS_STAGE + u.q * 4096);
; #pragma unroll
;         for (int bj = 0; bj < 2; ++bj) { const int cc = 128 * bj + wc * 32 + 8 * fq;
; #pragma unroll
;             EPI_LOOP_AM { const int r = 128 * ai + 64 * wr + 16 * m + fr;
;                 const f32x4 w0 = *(const LAS f32x4*)(blk + 256 + cc) * 0.25f, w1 = *(const LAS f32x4*)(blk + 256 + cc + 4) * 0.25f, b0 = *(const LAS f32x4*)(blk + 512 + cc), b1 = *(const LAS f32x4*)(blk + 512 + cc + 4);
;                 f32x4 y0 = (acc[ai][bj][m][0] * w0 + b0) * 32.f, y1 = (acc[ai][bj][m][1] * w1 + b1) * 32.f;
; #pragma unroll
;                 for (int j = 0; j < 4; ++j) { y0[j] = fminf(fmaxf(y0[j], -440.f), 440.f); y1[j] = fminf(fmaxf(y1[j], -440.f), 440.f); }
;                 int p0 = __builtin_amdgcn_cvt_pk_fp8_f32(y0[0], y0[1], 0, false); p0 = __builtin_amdgcn_cvt_pk_fp8_f32(y0[2], y0[3], p0, true);
;                 int p1 = __builtin_amdgcn_cvt_pk_fp8_f32(y1[0], y1[1], 0, false); p1 = __builtin_amdgcn_cvt_pk_fp8_f32(y1[2], y1[3], p1, true);
;                 *(GAS v2u*)(yr8 + ((size_t)rt * 256 + r) * D + c0 + 128 * bj) = (v2u){(unsigned)p0, (unsigned)p1}; EPI_FENCE; } }
;     }
	v_pk_fma_f32 v[32:33], v[32:33], v[44:45], v[188:189]
	v_med3_f32 v36, v36, s68, v140
	v_pk_mul_f32 v[32:33], v[32:33], s[18:19] op_sel_hi:[1,0]
	v_med3_f32 v37, v37, s68, v140
	v_med3_f32 v40, v32, s68, v140
	v_med3_f32 v41, v33, s68, v140
	v_mov_b32_e32 v32, v129
	v_mov_b32_e32 v33, v129
	v_cvt_pk_fp8_f32 v32, v36, v37
	v_cvt_pk_fp8_f32 v33, v40, v41
	v_pk_fma_f32 v[38:39], v[38:39], v[52:53], v[186:187]
	v_pk_fma_f32 v[34:35], v[34:35], v[46:47], v[190:191]
	v_pk_mul_f32 v[38:39], v[38:39], s[18:19] op_sel_hi:[1,0]
	v_pk_mul_f32 v[34:35], v[34:35], s[18:19] op_sel_hi:[1,0]
	v_med3_f32 v38, v38, s68, v140
	v_med3_f32 v34, v34, s68, v140
	v_med3_f32 v36, v39, s68, v140
	v_med3_f32 v35, v35, s68, v140
	v_cvt_pk_fp8_f32 v32, v38, v36 op_sel:[0,0,1]
	v_cvt_pk_fp8_f32 v33, v34, v35 op_sel:[0,0,1]
	global_store_dwordx2 v[96:97], v[32:33], off offset:128
	s_waitcnt lgkmcnt(0)
	v_pk_mul_f32 v[44:45], v[178:179], s[16:17] op_sel_hi:[1,0]
	v_pk_mul_f32 v[46:47], v[176:177], s[16:17] op_sel_hi:[1,0]
	v_pk_mul_f32 v[36:37], v[180:181], s[16:17] op_sel_hi:[1,0]
	v_pk_fma_f32 v[28:29], v[28:29], v[46:47], v[184:185]
	v_pk_mul_f32 v[38:39], v[182:183], s[16:17] op_sel_hi:[1,0]
	v_pk_mul_f32 v[28:29], v[28:29], s[18:19] op_sel_hi:[1,0]
	s_waitcnt lgkmcnt(0)
	v_pk_fma_f32 v[24:25], v[24:25], v[36:37], v[188:189]
	v_med3_f32 v28, v28, s68, v140
	v_pk_mul_f32 v[24:25], v[24:25], s[18:19] op_sel_hi:[1,0]
	v_med3_f32 v29, v29, s68, v140
	v_med3_f32 v32, v24, s68, v140
	v_med3_f32 v33, v25, s68, v140
	v_mov_b32_e32 v24, v129
	v_mov_b32_e32 v25, v129
	v_cvt_pk_fp8_f32 v24, v28, v29
	v_cvt_pk_fp8_f32 v25, v32, v33
	v_pk_fma_f32 v[30:31], v[30:31], v[44:45], v[186:187]
	v_pk_fma_f32 v[26:27], v[26:27], v[38:39], v[190:191]
	v_pk_mul_f32 v[30:31], v[30:31], s[18:19] op_sel_hi:[1,0]
	v_pk_mul_f32 v[26:27], v[26:27], s[18:19] op_sel_hi:[1,0]
	v_med3_f32 v30, v30, s68, v140
	v_med3_f32 v26, v26, s68, v140
	v_med3_f32 v28, v31, s68, v140
	v_med3_f32 v27, v27, s68, v140
	v_cvt_pk_fp8_f32 v24, v30, v28 op_sel:[0,0,1]
	v_cvt_pk_fp8_f32 v25, v26, v27 op_sel:[0,0,1]
	global_store_dwordx2 v[88:89], v[24:25], off offset:128
	s_waitcnt lgkmcnt(0)
	v_pk_mul_f32 v[36:37], v[178:179], s[16:17] op_sel_hi:[1,0]
	v_pk_mul_f32 v[38:39], v[176:177], s[16:17] op_sel_hi:[1,0]
	v_pk_mul_f32 v[28:29], v[180:181], s[16:17] op_sel_hi:[1,0]
	v_pk_fma_f32 v[20:21], v[20:21], v[38:39], v[184:185]
	v_pk_mul_f32 v[30:31], v[182:183], s[16:17] op_sel_hi:[1,0]
	v_pk_mul_f32 v[20:21], v[20:21], s[18:19] op_sel_hi:[1,0]
	s_waitcnt lgkmcnt(0)
	v_pk_fma_f32 v[16:17], v[16:17], v[28:29], v[188:189]
	v_med3_f32 v20, v20, s68, v140
	v_pk_mul_f32 v[16:17], v[16:17], s[18:19] op_sel_hi:[1,0]
	v_med3_f32 v21, v21, s68, v140
	v_med3_f32 v24, v16, s68, v140
	v_med3_f32 v25, v17, s68, v140
	v_mov_b32_e32 v16, v129
	v_mov_b32_e32 v17, v129
	v_cvt_pk_fp8_f32 v16, v20, v21
	v_cvt_pk_fp8_f32 v17, v24, v25
	v_pk_fma_f32 v[22:23], v[22:23], v[36:37], v[186:187]
	v_pk_fma_f32 v[18:19], v[18:19], v[30:31], v[190:191]
	v_pk_mul_f32 v[22:23], v[22:23], s[18:19] op_sel_hi:[1,0]
	v_pk_mul_f32 v[18:19], v[18:19], s[18:19] op_sel_hi:[1,0]
	v_med3_f32 v22, v22, s68, v140
	v_med3_f32 v18, v18, s68, v140
	v_med3_f32 v20, v23, s68, v140
	v_med3_f32 v19, v19, s68, v140
	v_cvt_pk_fp8_f32 v16, v22, v20 op_sel:[0,0,1]
	v_cvt_pk_fp8_f32 v17, v18, v19 op_sel:[0,0,1]
	global_store_dwordx2 v[80:81], v[16:17], off offset:128
	s_waitcnt lgkmcnt(0)
	v_pk_mul_f32 v[28:29], v[178:179], s[16:17] op_sel_hi:[1,0]
	v_pk_mul_f32 v[30:31], v[176:177], s[16:17] op_sel_hi:[1,0]
	v_pk_mul_f32 v[20:21], v[180:181], s[16:17] op_sel_hi:[1,0]
	v_pk_fma_f32 v[12:13], v[12:13], v[30:31], v[184:185]
	v_pk_mul_f32 v[22:23], v[182:183], s[16:17] op_sel_hi:[1,0]
	v_pk_mul_f32 v[12:13], v[12:13], s[18:19] op_sel_hi:[1,0]
	s_waitcnt lgkmcnt(0)
	v_pk_fma_f32 v[8:9], v[8:9], v[20:21], v[188:189]
	v_med3_f32 v12, v12, s68, v140
	v_pk_mul_f32 v[8:9], v[8:9], s[18:19] op_sel_hi:[1,0]
	v_med3_f32 v13, v13, s68, v140
	v_med3_f32 v16, v8, s68, v140
	v_med3_f32 v17, v9, s68, v140
	v_mov_b32_e32 v8, v129
	v_mov_b32_e32 v9, v129
	v_cvt_pk_fp8_f32 v8, v12, v13
	v_cvt_pk_fp8_f32 v9, v16, v17
	v_pk_fma_f32 v[14:15], v[14:15], v[28:29], v[186:187]
	v_pk_fma_f32 v[10:11], v[10:11], v[22:23], v[190:191]
	v_pk_mul_f32 v[14:15], v[14:15], s[18:19] op_sel_hi:[1,0]
	v_pk_mul_f32 v[10:11], v[10:11], s[18:19] op_sel_hi:[1,0]
	v_med3_f32 v14, v14, s68, v140
	v_med3_f32 v10, v10, s68, v140
	v_med3_f32 v12, v15, s68, v140
	v_med3_f32 v11, v11, s68, v140
	v_cvt_pk_fp8_f32 v8, v14, v12 op_sel:[0,0,1]
	v_cvt_pk_fp8_f32 v9, v10, v11 op_sel:[0,0,1]
	global_store_dwordx2 v[72:73], v[8:9], off offset:128
	s_waitcnt lgkmcnt(0)
	v_pk_mul_f32 v[20:21], v[178:179], s[16:17] op_sel_hi:[1,0]
	v_pk_mul_f32 v[22:23], v[176:177], s[16:17] op_sel_hi:[1,0]
	v_pk_mul_f32 v[12:13], v[180:181], s[16:17] op_sel_hi:[1,0]
	v_pk_fma_f32 v[4:5], v[4:5], v[22:23], v[184:185]
	v_pk_mul_f32 v[14:15], v[182:183], s[16:17] op_sel_hi:[1,0]
	v_pk_mul_f32 v[4:5], v[4:5], s[18:19] op_sel_hi:[1,0]
	s_waitcnt lgkmcnt(0)
	v_pk_fma_f32 v[0:1], v[0:1], v[12:13], v[188:189]
	v_med3_f32 v4, v4, s68, v140
	v_pk_mul_f32 v[0:1], v[0:1], s[18:19] op_sel_hi:[1,0]
	v_med3_f32 v5, v5, s68, v140
	v_med3_f32 v8, v0, s68, v140
	v_med3_f32 v9, v1, s68, v140
	v_mov_b32_e32 v0, v129
	v_mov_b32_e32 v1, v129
	v_cvt_pk_fp8_f32 v0, v4, v5
	v_cvt_pk_fp8_f32 v1, v8, v9
	v_pk_fma_f32 v[6:7], v[6:7], v[20:21], v[186:187]
	v_pk_fma_f32 v[2:3], v[2:3], v[14:15], v[190:191]
	v_pk_mul_f32 v[6:7], v[6:7], s[18:19] op_sel_hi:[1,0]
	v_pk_mul_f32 v[2:3], v[2:3], s[18:19] op_sel_hi:[1,0]
	v_med3_f32 v6, v6, s68, v140
	v_med3_f32 v2, v2, s68, v140
	v_med3_f32 v4, v7, s68, v140
	v_med3_f32 v3, v3, s68, v140
	v_cvt_pk_fp8_f32 v0, v6, v4 op_sel:[0,0,1]
	v_cvt_pk_fp8_f32 v1, v2, v3 op_sel:[0,0,1]
	global_store_dwordx2 v[64:65], v[0:1], off offset:128
	s_andn2_b64 vcc, exec, s[40:41]
	s_cbranch_vccnz .LBB0_1741
	s_andn2_b64 vcc, exec, s[8:9]
	s_cbranch_vccnz .LBB0_1714
	s_barrier
	s_branch .LBB0_1714
